# baseline (speedup 1.0000x reference)
.LBB9_23:
	s_or_b64 exec, exec, s[30:31]
	s_waitcnt vmcnt(0)
	v_mov_b32_e32 v128, 0
	v_mov_b32_e32 v0, 0
	s_xor_b64 s[30:31], s[34:35], -1
	s_mov_b32 s14, 0
	s_mov_b32 s34, 0
	s_mov_b32 s35, 0
	v_mov_b32_e32 v1, v0
	v_mov_b32_e32 v2, v0
	v_mov_b32_e32 v3, v0
	v_mov_b32_e32 v4, v0
	v_mov_b32_e32 v5, v0
	v_mov_b32_e32 v6, v0
	v_mov_b32_e32 v7, v0
	v_mov_b32_e32 v8, v0
	v_mov_b32_e32 v9, v0
	v_mov_b32_e32 v10, v0
	v_mov_b32_e32 v11, v0
	v_mov_b32_e32 v12, v0
	v_mov_b32_e32 v13, v0
	v_mov_b32_e32 v14, v0
	v_mov_b32_e32 v15, v0
	v_mov_b32_e32 v48, v0
	v_mov_b32_e32 v49, v0
	v_mov_b32_e32 v50, v0
	v_mov_b32_e32 v51, v0
	v_mov_b32_e32 v52, v0
	v_mov_b32_e32 v53, v0
	v_mov_b32_e32 v54, v0
	v_mov_b32_e32 v55, v0
	v_mov_b32_e32 v56, v0
	v_mov_b32_e32 v57, v0
	v_mov_b32_e32 v58, v0
	v_mov_b32_e32 v59, v0
	v_mov_b32_e32 v60, v0
	v_mov_b32_e32 v61, v0
	v_mov_b32_e32 v62, v0
	v_mov_b32_e32 v63, v0
	v_mov_b32_e32 v16, v0
	v_mov_b32_e32 v17, v0
	v_mov_b32_e32 v18, v0
	v_mov_b32_e32 v19, v0
	v_mov_b32_e32 v20, v0
	v_mov_b32_e32 v21, v0
	v_mov_b32_e32 v22, v0
	v_mov_b32_e32 v23, v0
	v_mov_b32_e32 v24, v0
	v_mov_b32_e32 v25, v0
	v_mov_b32_e32 v26, v0
	v_mov_b32_e32 v27, v0
	v_mov_b32_e32 v28, v0
	v_mov_b32_e32 v29, v0
	v_mov_b32_e32 v30, v0
	v_mov_b32_e32 v31, v0
	v_mov_b32_e32 v80, v0
	v_mov_b32_e32 v81, v0
	v_mov_b32_e32 v82, v0
	v_mov_b32_e32 v83, v0
	v_mov_b32_e32 v84, v0
	v_mov_b32_e32 v85, v0
	v_mov_b32_e32 v86, v0
	v_mov_b32_e32 v87, v0
	v_mov_b32_e32 v88, v0
	v_mov_b32_e32 v89, v0
	v_mov_b32_e32 v90, v0
	v_mov_b32_e32 v91, v0
	v_mov_b32_e32 v92, v0
	v_mov_b32_e32 v93, v0
	v_mov_b32_e32 v94, v0
	v_mov_b32_e32 v95, v0
	v_mov_b32_e32 v32, v0
	v_mov_b32_e32 v33, v0
	v_mov_b32_e32 v34, v0
	v_mov_b32_e32 v35, v0
	v_mov_b32_e32 v36, v0
	v_mov_b32_e32 v37, v0
	v_mov_b32_e32 v38, v0
	v_mov_b32_e32 v39, v0
	v_mov_b32_e32 v40, v0
	v_mov_b32_e32 v41, v0
	v_mov_b32_e32 v42, v0
	v_mov_b32_e32 v43, v0
	v_mov_b32_e32 v44, v0
	v_mov_b32_e32 v45, v0
	v_mov_b32_e32 v46, v0
	v_mov_b32_e32 v47, v0
	v_mov_b32_e32 v96, v0
	v_mov_b32_e32 v97, v0
	v_mov_b32_e32 v98, v0
	v_mov_b32_e32 v99, v0
	v_mov_b32_e32 v100, v0
	v_mov_b32_e32 v101, v0
	v_mov_b32_e32 v102, v0
	v_mov_b32_e32 v103, v0
	v_mov_b32_e32 v104, v0
	v_mov_b32_e32 v105, v0
	v_mov_b32_e32 v106, v0
	v_mov_b32_e32 v107, v0
	v_mov_b32_e32 v108, v0
	v_mov_b32_e32 v109, v0
	v_mov_b32_e32 v110, v0
	v_mov_b32_e32 v111, v0
	v_mov_b32_e32 v64, v0
	v_mov_b32_e32 v65, v0
	v_mov_b32_e32 v66, v0
	v_mov_b32_e32 v67, v0
	v_mov_b32_e32 v68, v0
	v_mov_b32_e32 v69, v0
	v_mov_b32_e32 v70, v0
	v_mov_b32_e32 v71, v0
	v_mov_b32_e32 v72, v0
	v_mov_b32_e32 v73, v0
	v_mov_b32_e32 v74, v0
	v_mov_b32_e32 v75, v0
	v_mov_b32_e32 v76, v0
	v_mov_b32_e32 v77, v0
	v_mov_b32_e32 v78, v0
	v_mov_b32_e32 v79, v0
	v_mov_b32_e32 v112, v0
	v_mov_b32_e32 v113, v0
	v_mov_b32_e32 v114, v0
	v_mov_b32_e32 v115, v0
	v_mov_b32_e32 v116, v0
	v_mov_b32_e32 v117, v0
	v_mov_b32_e32 v118, v0
	v_mov_b32_e32 v119, v0
	v_mov_b32_e32 v120, v0
	v_mov_b32_e32 v121, v0
	v_mov_b32_e32 v122, v0
	v_mov_b32_e32 v123, v0
	v_mov_b32_e32 v124, v0
	v_mov_b32_e32 v125, v0
	v_mov_b32_e32 v126, v0
	v_mov_b32_e32 v127, v0
	v_mov_b32_e32 v129, v128
	v_mov_b32_e32 v130, v128
	v_mov_b32_e32 v131, v128
	v_mov_b32_e32 v140, v128
	v_mov_b32_e32 v141, v128
	v_mov_b32_e32 v142, v128
	v_mov_b32_e32 v143, v128
	v_mov_b32_e32 v144, v128
	v_mov_b32_e32 v145, v128
	v_mov_b32_e32 v146, v128
	v_mov_b32_e32 v147, v128
	v_mov_b32_e32 v148, v128
	v_mov_b32_e32 v149, v128
	v_mov_b32_e32 v150, v128
	v_mov_b32_e32 v151, v128
	v_mov_b32_e32 v132, v128
	v_mov_b32_e32 v133, v128
	v_mov_b32_e32 v134, v128
	v_mov_b32_e32 v135, v128
	v_mov_b32_e32 v136, v128
	v_mov_b32_e32 v137, v128
	v_mov_b32_e32 v138, v128
	v_mov_b32_e32 v139, v128
	s_add_i32 s50, s34, -9
	s_cmp_gt_i32 s34, 8
	s_cselect_b64 s[36:37], -1, 0
	s_and_b64 s[38:39], s[36:37], exec
	s_cselect_b32 s38, s50, s34
	s_cmp_lg_u64 s[36:37], 0
	s_mul_hi_i32 s37, s38, 0x55555556
	s_addc_u32 s36, s35, 0
	s_lshr_b32 s39, s37, 31
	s_add_i32 s37, s37, s39
	s_mul_i32 s39, s37, -3
	s_add_i32 s39, s39, s38
	s_waitcnt lgkmcnt(0)
	s_barrier
	s_branch .LBB9_25
.LBB9_24:
	v_and_b32_e32 v239, 7, v239
	s_waitcnt lgkmcnt(0)
	v_mfma_f32_32x32x16_f16 v[112:127], v[156:159], v[140:143], v[112:127]
	v_add_u32_e32 v132, v237, v221
	v_bitop3_b32 v240, v239, v238, 4 bitop3:0x1e
	v_lshl_add_u32 v252, v240, 4, v160
	v_mfma_f32_32x32x16_f16 v[96:111], v[152:155], v[140:143], v[96:111]
	v_mfma_f32_32x32x16_f16 v[80:95], v[148:151], v[140:143], v[80:95]
	v_mfma_f32_32x32x16_f16 v[48:63], v[144:147], v[140:143], v[48:63]
	v_bitop3_b32 v140, v239, v238, 2 bitop3:0x1e
	v_mfma_f32_32x32x16_f16 v[16:31], v[148:151], v[136:139], v[16:31]
	v_lshl_add_u32 v148, v140, 4, v160
	v_mfma_f32_32x32x16_f16 v[64:79], v[156:159], v[136:139], v[64:79]
	v_add_u32_e32 v156, v237, v222
	v_mfma_f32_32x32x16_f16 v[32:47], v[152:155], v[136:139], v[32:47]
	v_mfma_f32_32x32x16_f16 v[0:15], v[144:147], v[136:139], v[0:15]
	ds_read_b128 v[136:139], v148
	ds_read_b128 v[140:143], v148 offset:4608
	ds_read_b128 v[144:147], v148 offset:9216
	ds_read_b128 v[148:151], v148 offset:13824
	ds_read_b128 v[128:131], v132 offset:41472
	ds_read_b128 v[132:135], v132 offset:45568
	ds_read_b128 v[240:243], v252
	ds_read_b128 v[244:247], v252 offset:4608
	ds_read_b128 v[248:251], v252 offset:9216
	ds_read_b128 v[252:255], v252 offset:13824
	ds_read_b128 v[152:155], v156 offset:41472
	ds_read_b128 v[156:159], v156 offset:45568
	s_waitcnt lgkmcnt(0)
	v_mfma_f32_32x32x16_f16 v[112:127], v[136:139], v[128:131], v[112:127]
	v_mfma_f32_32x32x16_f16 v[64:79], v[136:139], v[132:135], v[64:79]
	v_mfma_f32_32x32x16_f16 v[96:111], v[140:143], v[128:131], v[96:111]
	v_mfma_f32_32x32x16_f16 v[32:47], v[140:143], v[132:135], v[32:47]
	v_mfma_f32_32x32x16_f16 v[80:95], v[144:147], v[128:131], v[80:95]
	v_mfma_f32_32x32x16_f16 v[16:31], v[144:147], v[132:135], v[16:31]
	v_mfma_f32_32x32x16_f16 v[48:63], v[148:151], v[128:131], v[48:63]
	v_bitop3_b32 v128, v239, v238, 6 bitop3:0x1e
	v_add_u32_e32 v129, v237, v223
	v_lshl_add_u32 v128, v128, 4, v160
	v_mfma_f32_32x32x16_f16 v[0:15], v[148:151], v[132:135], v[0:15]
	ds_read_b128 v[136:139], v129 offset:41472
	ds_read_b128 v[132:135], v129 offset:45568
	ds_read_b128 v[148:151], v128
	ds_read_b128 v[144:147], v128 offset:4608
	ds_read_b128 v[140:143], v128 offset:9216
	ds_read_b128 v[128:131], v128 offset:13824
	v_mfma_f32_32x32x16_f16 v[112:127], v[240:243], v[152:155], v[112:127]
	v_mfma_f32_32x32x16_f16 v[64:79], v[240:243], v[156:159], v[64:79]
	v_mfma_f32_32x32x16_f16 v[96:111], v[244:247], v[152:155], v[96:111]
	v_mfma_f32_32x32x16_f16 v[32:47], v[244:247], v[156:159], v[32:47]
	v_mfma_f32_32x32x16_f16 v[80:95], v[248:251], v[152:155], v[80:95]
	v_mfma_f32_32x32x16_f16 v[16:31], v[248:251], v[156:159], v[16:31]
	v_mfma_f32_32x32x16_f16 v[48:63], v[252:255], v[152:155], v[48:63]
	v_mfma_f32_32x32x16_f16 v[0:15], v[252:255], v[156:159], v[0:15]
	s_cmp_gt_i32 s34, 7
	s_cselect_b64 s[38:39], -1, 0
	s_and_b64 s[50:51], s[38:39], exec
	s_cselect_b32 s14, -8, 1
	s_cmp_lg_u64 s[38:39], 0
	s_addc_u32 s35, s35, 0
	s_add_i32 s34, s14, s34
	s_mov_b32 s14, s36
	s_add_i32 s50, s34, -9
	s_cmp_gt_i32 s34, 8
	s_cselect_b64 s[36:37], -1, 0
	s_and_b64 s[38:39], s[36:37], exec
	s_cselect_b32 s38, s50, s34
	s_cmp_lg_u64 s[36:37], 0
	s_mul_hi_i32 s37, s38, 0x55555556
	s_addc_u32 s36, s35, 0
	s_lshr_b32 s39, s37, 31
	s_add_i32 s37, s37, s39
	s_mul_i32 s39, s37, -3
	s_add_i32 s39, s39, s38
	s_cmp_lg_u32 s14, 9
	s_waitcnt vmcnt(0)
	s_waitcnt lgkmcnt(0)
	s_barrier
	s_cbranch_scc0 .LBB9_1
.LBB9_25:
	s_waitcnt lgkmcnt(0)
	v_mfma_f32_32x32x16_f16 v[96:111], v[144:147], v[136:139], v[96:111]
	v_lshl_or_b32 v238, s36, 3, v195
	s_mov_b32 s36, 9
	v_mfma_f32_32x32x16_f16 v[32:47], v[144:147], v[132:135], v[32:47]
	v_add_u32_e32 v145, s39, v217
	v_add_u32_e32 v144, s37, v218
	v_lshrrev_b32_e32 v146, 1, v145
	s_lshl_b32 s37, s14, 14
	v_lshl_add_u32 v239, v144, 2, v146
	v_mul_lo_u32 v144, v144, 18
	s_and_b32 s37, s37, 0x4000
	v_add_lshl_u32 v160, v145, v144, 7
	v_or_b32_e32 v237, s37, v219
	v_bitop3_b32 v144, v239, v238, 7 bitop3:0x6c
	v_mfma_f32_32x32x16_f16 v[112:127], v[148:151], v[136:139], v[112:127]
	v_add_u32_e32 v145, v237, v220
	v_lshl_add_u32 v144, v144, 4, v160
	s_cmp_eq_u32 s14, 8
	v_mfma_f32_32x32x16_f16 v[64:79], v[148:151], v[132:135], v[64:79]
	v_mfma_f32_32x32x16_f16 v[80:95], v[140:143], v[136:139], v[80:95]
	v_mfma_f32_32x32x16_f16 v[16:31], v[140:143], v[132:135], v[16:31]
	v_mfma_f32_32x32x16_f16 v[48:63], v[128:131], v[136:139], v[48:63]
	ds_read_b128 v[140:143], v145 offset:41472
	ds_read_b128 v[136:139], v145 offset:45568
	ds_read_b128 v[156:159], v144
	ds_read_b128 v[152:155], v144 offset:4608
	ds_read_b128 v[148:151], v144 offset:9216
	ds_read_b128 v[144:147], v144 offset:13824
	v_mfma_f32_32x32x16_f16 v[0:15], v[128:131], v[132:135], v[0:15]
	s_cbranch_scc1 .LBB9_24
	s_add_i32 s36, s14, 1
	s_lshl_b32 s14, s36, 14
	s_and_b32 s37, s14, 0x4000
	v_or_b32_e32 v134, s37, v194
	v_add_u32_e32 v240, 0xa200, v134
	v_lshl_add_u64 v[128:129], v[164:165], 0, s[14:15]
	v_add_u32_e32 v243, 0xb200, v134
	v_readfirstlane_b32 s14, v240
	v_add_u32_e32 v242, 0xc200, v134
	s_mov_b32 m0, s14
	v_readfirstlane_b32 s14, v243
	v_add_u32_e32 v241, 0xd200, v134
	v_lshl_add_u64 v[134:135], v[128:129], 0, s[16:17]
	global_load_lds_dwordx4 v[128:129], off
	s_mov_b32 m0, s14
	v_readfirstlane_b32 s14, v242
	v_lshl_add_u64 v[132:133], v[128:129], 0, s[18:19]
	global_load_lds_dwordx4 v[134:135], off
	s_mov_b32 m0, s14
	v_readfirstlane_b32 s14, v241
	v_lshl_add_u64 v[130:131], v[128:129], 0, s[20:21]
	global_load_lds_dwordx4 v[132:133], off
	s_mov_b32 m0, s14
	s_nop 0
	global_load_lds_dwordx4 v[130:131], off
	s_branch .LBB9_24
.LBB9_31:
	s_endpgm
	s_endpgm
	s_endpgm
	s_endpgm
	s_endpgm
	s_endpgm
	s_endpgm
	s_endpgm
	s_endpgm
	s_endpgm
	s_endpgm
	s_endpgm
	s_endpgm
	s_endpgm
	s_endpgm
	s_endpgm
	s_endpgm
	s_endpgm
	s_endpgm
	s_endpgm
	.section	.rodata,"a",@progbits
	.p2align	6, 0x0

.LBB10_5:
	v_add_u32_e32 v130, v233, v229
	s_waitcnt lgkmcnt(0)
	v_mfma_f32_32x32x16_f16 v[66:81], v[150:153], v[186:189], v[66:81]
	ds_read_b128 v[174:177], v130
	ds_read_b128 v[166:169], v130 offset:4096
	v_and_b32_e32 v130, 15, v154
	v_bitop3_b32 v131, v130, v232, 4 bitop3:0x1e
	v_lshl_add_u32 v131, v131, 4, v231
	v_bitop3_b32 v130, v130, v232, 6 bitop3:0x1e
	v_lshl_add_u32 v130, v130, 4, v231
	v_mfma_f32_32x32x16_f16 v[34:49], v[150:153], v[190:193], v[34:49]
	ds_read_b128 v[170:173], v131
	ds_read_b128 v[162:165], v131 offset:9216
	v_mfma_f32_32x32x16_f16 v[82:97], v[138:141], v[186:189], v[82:97]
	ds_read_b128 v[158:161], v131 offset:18432
	ds_read_b128 v[154:157], v131 offset:27648
	v_add_u32_e32 v131, v233, v230
	v_mfma_f32_32x32x16_f16 v[2:17], v[138:141], v[190:193], v[2:17]
	ds_read_b128 v[146:149], v131
	ds_read_b128 v[142:145], v131 offset:4096
	v_mfma_f32_32x32x16_f16 v[114:129], v[134:137], v[186:189], v[114:129]
	ds_read_b128 v[150:153], v130
	ds_read_b128 v[138:141], v130 offset:9216
	v_mfma_f32_32x32x16_f16 v[50:65], v[134:137], v[190:193], v[50:65]
	ds_read_b128 v[134:137], v130 offset:18432
	ds_read_b128 v[130:133], v130 offset:27648
	v_mfma_f32_32x32x16_f16 v[98:113], v[202:205], v[186:189], v[98:113]
	v_mfma_f32_32x32x16_f16 v[18:33], v[202:205], v[190:193], v[18:33]
	v_mfma_f32_32x32x16_f16 v[66:81], v[210:213], v[182:185], v[66:81]
	v_mfma_f32_32x32x16_f16 v[34:49], v[210:213], v[178:181], v[34:49]
	v_mfma_f32_32x32x16_f16 v[82:97], v[206:209], v[182:185], v[82:97]
	v_mfma_f32_32x32x16_f16 v[2:17], v[206:209], v[178:181], v[2:17]
	v_mfma_f32_32x32x16_f16 v[114:129], v[198:201], v[182:185], v[114:129]
	v_mfma_f32_32x32x16_f16 v[50:65], v[198:201], v[178:181], v[50:65]
	v_mfma_f32_32x32x16_f16 v[98:113], v[194:197], v[182:185], v[98:113]
	v_mfma_f32_32x32x16_f16 v[18:33], v[194:197], v[178:181], v[18:33]
	s_cmp_gt_i32 s14, 7
	s_cselect_b64 s[18:19], -1, 0
	s_and_b64 s[20:21], s[18:19], exec
	s_cselect_b32 s4, -8, 1
	s_cmp_lg_u64 s[18:19], 0
	s_addc_u32 s15, s15, 0
	s_add_i32 s14, s4, s14
	s_cmp_lg_u32 s16, 18
	s_mov_b32 s4, s16
	s_waitcnt vmcnt(0)
	s_waitcnt lgkmcnt(0)
	s_barrier
	s_cbranch_scc0 .LBB10_8

.LBB11_5:
	v_and_b32_e32 v120, 15, v112
	s_waitcnt lgkmcnt(0)
	v_mfma_f32_32x32x16_f16 v[50:65], v[86:89], v[82:85], v[50:65]
	v_add_u32_e32 v70, v110, v106
	v_bitop3_b32 v112, v120, v111, 4 bitop3:0x1e
	v_lshl_add_u32 v116, v112, 4, v109
	v_mfma_f32_32x32x16_f16 v[18:33], v[78:81], v[82:85], v[18:33]
	v_bitop3_b32 v82, v120, v111, 2 bitop3:0x1e
	v_mfma_f32_32x32x16_f16 v[2:17], v[78:81], v[74:77], v[2:17]
	v_lshl_add_u32 v78, v82, 4, v109
	v_mfma_f32_32x32x16_f16 v[34:49], v[86:89], v[74:77], v[34:49]
	ds_read_b128 v[74:77], v78
	ds_read_b128 v[78:81], v78 offset:18432
	ds_read_b128 v[66:69], v70
	ds_read_b128 v[70:73], v70 offset:4096
	v_add_u32_e32 v86, v110, v107
	ds_read_b128 v[112:115], v116
	ds_read_b128 v[116:119], v116 offset:18432
	ds_read_b128 v[82:85], v86
	ds_read_b128 v[86:89], v86 offset:4096
	s_waitcnt lgkmcnt(0)
	v_mfma_f32_32x32x16_f16 v[50:65], v[74:77], v[66:69], v[50:65]
	v_mfma_f32_32x32x16_f16 v[34:49], v[74:77], v[70:73], v[34:49]
	v_mfma_f32_32x32x16_f16 v[18:33], v[78:81], v[66:69], v[18:33]
	v_bitop3_b32 v66, v120, v111, 6 bitop3:0x1e
	v_add_u32_e32 v67, v110, v108
	v_lshl_add_u32 v66, v66, 4, v109
	v_mfma_f32_32x32x16_f16 v[2:17], v[78:81], v[70:73], v[2:17]
	ds_read_b128 v[74:77], v67
	ds_read_b128 v[70:73], v67 offset:4096
	ds_read_b128 v[78:81], v66
	ds_read_b128 v[66:69], v66 offset:18432
	v_mfma_f32_32x32x16_f16 v[50:65], v[112:115], v[82:85], v[50:65]
	v_mfma_f32_32x32x16_f16 v[34:49], v[112:115], v[86:89], v[34:49]
	v_mfma_f32_32x32x16_f16 v[18:33], v[116:119], v[82:85], v[18:33]
	v_mfma_f32_32x32x16_f16 v[2:17], v[116:119], v[86:89], v[2:17]
	s_cmp_gt_i32 s18, 6
	s_cselect_b64 s[20:21], -1, 0
	s_and_b64 s[22:23], s[20:21], exec
	s_cselect_b32 s1, -7, 2
	s_cmp_lg_u64 s[20:21], 0
	s_addc_u32 s19, s19, 0
	s_add_i32 s18, s1, s18
	s_cmp_eq_u32 s0, 18
	s_mov_b32 s6, s0
	s_waitcnt vmcnt(0)
	s_waitcnt lgkmcnt(0)
	s_barrier
	s_cbranch_scc1 .LBB11_8
